# v53: K-frag LDS read hoist (sub-tile1 reads issued in sub-tile0) extended to diff and NSA tile loops
# baseline (speedup 1.0000x reference)
.LBB0_447:
	s_add_i32 s2, s26, s23
	s_and_b32 s3, s30, 0x18000
	s_add_i32 s3, s3, 0
	s_add_i32 s33, s3, s27
	v_add_u32_e32 v2, s33, v162
	v_add_u32_e32 v4, s33, v164
	v_add_u32_e32 v5, s33, v165
	v_add_u32_e32 v70, s33, v166
	s_ashr_i32 s33, s31, 2
	v_cvt_f32_i32_e32 v170, s33
	v_add_u32_e32 v106, s3, v160
	s_add_i32 s3, s2, 0x7e0
	v_add_u32_e32 v169, 0x4000, v106
	s_cmp_gt_i32 s3, s28
	v_add_u32_e32 v174, v2, v145
	v_add_u32_e32 v173, v4, v145
	v_add_u32_e32 v172, v5, v145
	v_add_u32_e32 v171, v70, v145
	s_barrier
	s_cbranch_scc1 .Lkpre_skip_d
	ds_read_b128 v[70:73], v174 offset:4096
	ds_read_b128 v[188:191], v173 offset:4096
	ds_read_b128 v[192:195], v172 offset:4096
	ds_read_b128 v[202:205], v171 offset:4096
	s_and_b32 s3, s3, 0xe0
	v_or_b32_e32 v2, s3, v159
	v_cvt_f32_ubyte0_e32 v2, v2
	v_and_b32_e32 v2, 0x7fff0000, v2
	v_or_b32_sdwa v2, v2, v170 dst_sel:DWORD dst_unused:UNUSED_PAD src0_sel:DWORD src1_sel:WORD_1
	v_cndmask_b32_e64 v2, 0, v2, s[36:37]
	v_mov_b32_e32 v4, v3
	s_waitcnt lgkmcnt(3)
	s_setprio 1
	v_mfma_f32_32x32x16_bf16 v[70:85], v[70:73], v[86:89], 0
	v_mov_b32_e32 v5, v3
	s_add_i32 s3, s2, 0x7ff
	s_cmp_ge_i32 s19, s3
	s_cselect_b64 s[40:41], -1, 0
	s_add_i32 s3, s29, 0xffffffa0
	s_cmp_lt_i32 s3, 0x3fffffe1
	v_add_u32_e32 v175, v169, v150
	s_waitcnt lgkmcnt(2)
	v_mfma_f32_32x32x16_bf16 v[70:85], v[188:191], v[90:93], v[70:85]
	s_cselect_b64 s[42:43], -1, 0
	s_and_b64 s[40:41], s[40:41], s[42:43]
	s_and_b64 vcc, exec, s[40:41]
	s_waitcnt lgkmcnt(1)
	v_mfma_f32_32x32x16_bf16 v[70:85], v[192:195], v[94:97], v[70:85]
	s_waitcnt lgkmcnt(0)
	v_mfma_f32_32x32x16_bf16 v[70:85], v[202:205], v[98:101], v[70:85]
	v_mfma_f32_32x32x16_bf16 v[70:85], v[2:5], v[102:105], v[70:85]
	v_add3_u32 v2, v106, v142, s68
	v_add_u32_e32 v4, v169, v146
	v_add_u32_e32 v5, v169, v148
	ds_read_b64_tr_b16 v[134:135], v2
	ds_read_b64_tr_b16 v[136:137], v2 offset:2048
	ds_read_b64_tr_b16 v[130:131], v4
	ds_read_b64_tr_b16 v[132:133], v4 offset:2048
	ds_read_b64_tr_b16 v[126:127], v5
	ds_read_b64_tr_b16 v[128:129], v5 offset:2048
	ds_read_b64_tr_b16 v[122:123], v175
	ds_read_b64_tr_b16 v[124:125], v175 offset:2048
	ds_read_b64_tr_b16 v[118:119], v2 offset:4096
	ds_read_b64_tr_b16 v[120:121], v2 offset:6144
	ds_read_b64_tr_b16 v[114:115], v4 offset:4096
	ds_read_b64_tr_b16 v[116:117], v4 offset:6144
	ds_read_b64_tr_b16 v[110:111], v5 offset:4096
	ds_read_b64_tr_b16 v[112:113], v5 offset:6144
	ds_read_b64_tr_b16 v[106:107], v175 offset:4096
	ds_read_b64_tr_b16 v[108:109], v175 offset:6144
	ds_read_b128 v[188:191], v174
	ds_read_b128 v[192:195], v173
	ds_read_b128 v[202:205], v172
	s_cbranch_vccnz .LBB0_452
	v_add_u32_e32 v2, s29, v161
	v_add_u32_e32 v4, 0xffffffa0, v2
	v_cmp_gt_u32_e32 vcc, 2.0, v4
	v_add_u32_e32 v4, s23, v163
	v_add_u32_e32 v4, 0x60, v4
	s_nop 2
	v_cndmask_b32_e32 v70, v197, v70, vcc
	v_cmp_lt_u32_e32 vcc, s75, v4
	v_add_u32_e32 v4, 0xffffff9e, v2
	s_nop 0
	v_cndmask_b32_e32 v71, v197, v71, vcc
	v_cmp_gt_u32_e32 vcc, 2.0, v4
	v_add_u32_e32 v4, 0xffffff9d, v2
	s_nop 0
	v_cndmask_b32_e32 v72, v197, v72, vcc
	v_cmp_gt_u32_e32 vcc, 2.0, v4
	v_add_u32_e32 v4, 0xffffff98, v2
	s_nop 0
	v_cndmask_b32_e32 v73, v197, v73, vcc
	v_cmp_gt_u32_e32 vcc, 2.0, v4
	v_add_u32_e32 v4, 0xffffff97, v2
	s_nop 0
	v_cndmask_b32_e32 v74, v197, v74, vcc
	v_cmp_gt_u32_e32 vcc, 2.0, v4
	v_add_u32_e32 v4, 0xffffff96, v2
	s_nop 0
	v_cndmask_b32_e32 v75, v197, v75, vcc
	v_cmp_gt_u32_e32 vcc, 2.0, v4
	v_add_u32_e32 v4, 0xffffff95, v2
	s_nop 0
	v_cndmask_b32_e32 v76, v197, v76, vcc
	v_cmp_gt_u32_e32 vcc, 2.0, v4
	v_add_u32_e32 v4, 0xffffff90, v2
	s_nop 0
	v_cndmask_b32_e32 v77, v197, v77, vcc
	v_cmp_gt_u32_e32 vcc, 2.0, v4
	v_add_u32_e32 v4, 0xffffff8f, v2
	s_nop 0
	v_cndmask_b32_e32 v78, v197, v78, vcc
	v_cmp_gt_u32_e32 vcc, 2.0, v4
	v_add_u32_e32 v4, 0xffffff8e, v2
	s_nop 0
	v_cndmask_b32_e32 v79, v197, v79, vcc
	v_cmp_gt_u32_e32 vcc, 2.0, v4
	v_add_u32_e32 v4, 0xffffff8d, v2
	s_nop 0
	v_cndmask_b32_e32 v80, v197, v80, vcc
	v_cmp_gt_u32_e32 vcc, 2.0, v4
	v_add_u32_e32 v4, 0xffffff88, v2
	s_nop 0
	v_cndmask_b32_e32 v81, v197, v81, vcc
	v_cmp_gt_u32_e32 vcc, 2.0, v4
	v_add_u32_e32 v4, 0xffffff87, v2
	s_nop 0
	v_cndmask_b32_e32 v82, v197, v82, vcc
	v_cmp_gt_u32_e32 vcc, 2.0, v4
	v_add_u32_e32 v4, 0xffffff86, v2
	v_add_u32_e32 v2, 0xffffff85, v2
	v_cndmask_b32_e32 v83, v197, v83, vcc
	v_cmp_gt_u32_e32 vcc, 2.0, v4
	s_nop 1
	v_cndmask_b32_e32 v84, v197, v84, vcc
	v_cmp_gt_u32_e32 vcc, 2.0, v2
	s_nop 1
	v_cndmask_b32_e32 v85, v197, v85, vcc

.Lring_issue_skip_2:
	s_add_i32 s3, s2, 0x7c0
	s_cmp_gt_i32 s3, s28
	s_cbranch_scc1 .LBB0_461
	ds_read_b128 v[134:137], v171
	s_and_b32 s3, s3, 0xc0
	v_or_b32_e32 v2, s3, v159
	v_cvt_f32_ubyte0_e32 v2, v2
	v_and_b32_e32 v2, 0x7fff0000, v2
	v_or_b32_sdwa v2, v2, v170 dst_sel:DWORD dst_unused:UNUSED_PAD src0_sel:DWORD src1_sel:WORD_1
	v_cndmask_b32_e64 v2, 0, v2, s[36:37]
	v_mov_b32_e32 v4, v3
	s_waitcnt lgkmcnt(1)
	s_setprio 1
	v_mfma_f32_32x32x16_bf16 v[70:85], v[188:191], v[86:89], 0
	v_mov_b32_e32 v5, v3
	s_addk_i32 s2, 0x7df
	s_cmp_ge_i32 s19, s2
	s_cselect_b64 s[2:3], -1, 0
	s_sub_i32 s33, s29, 64
	s_cmp_lt_i32 s33, 0x3fffffe1
	s_cselect_b64 s[40:41], -1, 0
	v_mfma_f32_32x32x16_bf16 v[70:85], v[192:195], v[90:93], v[70:85]
	s_and_b64 s[2:3], s[2:3], s[40:41]
	s_and_b64 vcc, exec, s[2:3]
	v_mfma_f32_32x32x16_bf16 v[70:85], v[202:205], v[94:97], v[70:85]
	s_waitcnt lgkmcnt(0)
	v_mfma_f32_32x32x16_bf16 v[70:85], v[134:137], v[98:101], v[70:85]
	v_mfma_f32_32x32x16_bf16 v[70:85], v[2:5], v[102:105], v[70:85]
	v_add_u32_e32 v2, v169, v142
	v_add_u32_e32 v4, v169, v152
	v_add_u32_e32 v5, v169, v154
	v_add_u32_e32 v169, v169, v156
	ds_read_b64_tr_b16 v[134:135], v2
	ds_read_b64_tr_b16 v[136:137], v2 offset:2048
	ds_read_b64_tr_b16 v[130:131], v4
	ds_read_b64_tr_b16 v[132:133], v4 offset:2048
	ds_read_b64_tr_b16 v[126:127], v5
	ds_read_b64_tr_b16 v[128:129], v5 offset:2048
	ds_read_b64_tr_b16 v[122:123], v169
	ds_read_b64_tr_b16 v[124:125], v169 offset:2048
	ds_read_b64_tr_b16 v[118:119], v2 offset:4096
	ds_read_b64_tr_b16 v[120:121], v2 offset:6144
	ds_read_b64_tr_b16 v[114:115], v4 offset:4096
	ds_read_b64_tr_b16 v[116:117], v4 offset:6144
	ds_read_b64_tr_b16 v[110:111], v5 offset:4096
	ds_read_b64_tr_b16 v[112:113], v5 offset:6144
	ds_read_b64_tr_b16 v[106:107], v169 offset:4096
	ds_read_b64_tr_b16 v[108:109], v169 offset:6144
	s_cbranch_vccnz .LBB0_458
	v_add_u32_e32 v2, s29, v161
	v_subrev_u32_e32 v4, 64, v2
	v_cmp_gt_u32_e32 vcc, 2.0, v4
	v_add3_u32 v4, v163, s23, 64
	s_nop 2
	v_cndmask_b32_e32 v70, v197, v70, vcc
	v_cmp_lt_u32_e32 vcc, s75, v4
	v_add_u32_e32 v4, 0xffffffbe, v2
	s_nop 0
	v_cndmask_b32_e32 v71, v197, v71, vcc
	v_cmp_gt_u32_e32 vcc, 2.0, v4
	v_add_u32_e32 v4, 0xffffffbd, v2
	s_nop 0
	v_cndmask_b32_e32 v72, v197, v72, vcc
	v_cmp_gt_u32_e32 vcc, 2.0, v4
	v_add_u32_e32 v4, 0xffffffb8, v2
	s_nop 0
	v_cndmask_b32_e32 v73, v197, v73, vcc
	v_cmp_gt_u32_e32 vcc, 2.0, v4
	v_add_u32_e32 v4, 0xffffffb7, v2
	s_nop 0
	v_cndmask_b32_e32 v74, v197, v74, vcc
	v_cmp_gt_u32_e32 vcc, 2.0, v4
	v_add_u32_e32 v4, 0xffffffb6, v2
	s_nop 0
	v_cndmask_b32_e32 v75, v197, v75, vcc
	v_cmp_gt_u32_e32 vcc, 2.0, v4
	v_add_u32_e32 v4, 0xffffffb5, v2
	s_nop 0
	v_cndmask_b32_e32 v76, v197, v76, vcc
	v_cmp_gt_u32_e32 vcc, 2.0, v4
	v_add_u32_e32 v4, 0xffffffb0, v2
	s_nop 0
	v_cndmask_b32_e32 v77, v197, v77, vcc
	v_cmp_gt_u32_e32 vcc, 2.0, v4
	v_add_u32_e32 v4, 0xffffffaf, v2
	s_nop 0
	v_cndmask_b32_e32 v78, v197, v78, vcc
	v_cmp_gt_u32_e32 vcc, 2.0, v4
	v_add_u32_e32 v4, 0xffffffae, v2
	s_nop 0
	v_cndmask_b32_e32 v79, v197, v79, vcc
	v_cmp_gt_u32_e32 vcc, 2.0, v4
	v_add_u32_e32 v4, 0xffffffad, v2
	s_nop 0
	v_cndmask_b32_e32 v80, v197, v80, vcc
	v_cmp_gt_u32_e32 vcc, 2.0, v4
	v_add_u32_e32 v4, 0xffffffa8, v2
	s_nop 0
	v_cndmask_b32_e32 v81, v197, v81, vcc
	v_cmp_gt_u32_e32 vcc, 2.0, v4
	v_add_u32_e32 v4, 0xffffffa7, v2
	s_nop 0
	v_cndmask_b32_e32 v82, v197, v82, vcc
	v_cmp_gt_u32_e32 vcc, 2.0, v4
	v_add_u32_e32 v4, 0xffffffa6, v2
	v_add_u32_e32 v2, 0xffffffa5, v2
	v_cndmask_b32_e32 v83, v197, v83, vcc
	v_cmp_gt_u32_e32 vcc, 2.0, v4
	s_nop 1
	v_cndmask_b32_e32 v84, v197, v84, vcc
	v_cmp_gt_u32_e32 vcc, 2.0, v2
	s_nop 1
	v_cndmask_b32_e32 v85, v197, v85, vcc

.LBB0_461:
	s_waitcnt lgkmcnt(0)
	s_add_i32 s30, s30, 0x8000
	s_add_i32 s22, s22, 1
	s_sub_i32 s23, s23, 64
	s_add_i32 s29, s29, 64
	s_cmp_eq_u32 s31, 0
	s_cbranch_scc0 .LBB0_439
	v_mov_b32_e32 v2, v167
	s_nop 1
	v_permlane32_swap_b32_e32 v167, v2
	v_add_f32_e32 v2, v167, v2
	v_div_scale_f32 v4, s[2:3], v2, v2, 1.0
	v_rcp_f32_e32 v5, v4
	s_cmp_eq_u32 s5, 0
	s_cselect_b64 s[2:3], -1, 0
	s_waitcnt vmcnt(0) lgkmcnt(0)
	s_cmpk_gt_i32 s61, 0xbff
	s_cbranch_scc1 .Lpf_dif_skip
	s_mul_hi_i32 s84, s61, 0x2aaaaaab
	s_lshr_b32 s84, s84, 4
	s_mul_i32 s85, s84, 0xffffffa0
	s_add_i32 s85, s85, s61
	v_readlane_b32 s87, v254, 7
	v_readlane_b32 s88, v253, 1
	v_readlane_b32 s89, v253, 2
	s_lshl_b32 s86, s61, 7
	s_and_b32 s86, s86, 0x380
	v_ashrrev_i32_e32 v246, 2, v0
	v_and_b32_e32 v246, -4, v246
	v_add_u32_e32 v246, s86, v246
	v_lshlrev_b32_e32 v248, 4, v0
	v_and_b32_e32 v248, 0xf0, v248
	s_lshl_b32 s87, s87, 5
	s_add_i32 s92, s84, s87
	s_mov_b32 s93, 0
	s_cmp_gt_i32 s85, 63
	s_cbranch_scc1 .Lpf_dif_w2
	s_load_dwordx2 s[90:91], s[88:89], 0xa0
	s_lshl_b64 s[92:93], s[92:93], 23
	v_lshlrev_b32_e32 v246, 13, v246
	s_lshl_b32 s86, s85, 4
	s_and_b32 s86, s86, 0xffffff80
	s_lshl_b32 s86, s86, 2
	v_add3_u32 v246, v246, v248, s86
	v_mov_b32_e32 v247, 0
	s_waitcnt lgkmcnt(0)
	s_add_u32 s90, s90, s92
	s_addc_u32 s91, s91, s93
	v_lshl_add_u64 v[246:247], s[90:91], 0, v[246:247]
	s_mov_b64 s[94:95], 0x2000
	v_lshl_add_u64 v[248:249], v[246:247], 0, s[94:95]
	global_load_dwordx4 v[148:151], v[248:249], off nt
	s_mov_b64 s[94:95], 0x4000
	v_lshl_add_u64 v[250:251], v[246:247], 0, s[94:95]
	global_load_dwordx4 v[168:171], v[250:251], off nt
	global_load_dwordx4 v[172:175], v[246:247], off nt
	global_load_dwordx4 v[176:179], v[246:247], off offset:256 nt
	s_mov_b64 s[94:95], 0x6000
	v_lshl_add_u64 v[248:249], v[246:247], 0, s[94:95]
	global_load_dwordx4 v[188:191], v[248:249], off nt
	s_mov_b64 s[94:95], 0x2000
	v_lshl_add_u64 v[250:251], v[246:247], 0, s[94:95]
	global_load_dwordx4 v[192:195], v[250:251], off offset:256 nt
	s_mov_b64 s[94:95], 0x4000
	v_lshl_add_u64 v[248:249], v[246:247], 0, s[94:95]
	global_load_dwordx4 v[202:205], v[248:249], off offset:256 nt
	s_mov_b64 s[94:95], 0x6000
	v_lshl_add_u64 v[250:251], v[246:247], 0, s[94:95]
	global_load_dwordx4 v[206:209], v[250:251], off offset:256 nt
	s_mov_b64 s[94:95], 0x1000
	v_lshl_add_u64 v[248:249], v[246:247], 0, s[94:95]
	global_load_dwordx4 v[210:213], v[248:249], off nt
	s_mov_b64 s[94:95], 0x3000
	v_lshl_add_u64 v[250:251], v[246:247], 0, s[94:95]
	global_load_dwordx4 v[214:217], v[250:251], off nt
	s_mov_b64 s[94:95], 0x5000
	v_lshl_add_u64 v[248:249], v[246:247], 0, s[94:95]
	global_load_dwordx4 v[222:225], v[248:249], off nt
	s_mov_b64 s[94:95], 0x7000
	v_lshl_add_u64 v[250:251], v[246:247], 0, s[94:95]
	global_load_dwordx4 v[226:229], v[250:251], off nt
	s_mov_b64 s[94:95], 0x1000
	v_lshl_add_u64 v[248:249], v[246:247], 0, s[94:95]
	global_load_dwordx4 v[230:233], v[248:249], off offset:256 nt
	s_mov_b64 s[94:95], 0x3000
	v_lshl_add_u64 v[250:251], v[246:247], 0, s[94:95]
	global_load_dwordx4 v[234:237], v[250:251], off offset:256 nt
	s_mov_b64 s[94:95], 0x5000
	v_lshl_add_u64 v[248:249], v[246:247], 0, s[94:95]
	global_load_dwordx4 v[238:241], v[248:249], off offset:256 nt
	s_mov_b64 s[94:95], 0x7000
	v_lshl_add_u64 v[250:251], v[246:247], 0, s[94:95]
	global_load_dwordx4 v[242:245], v[250:251], off offset:256 nt
	s_branch .Lpf_dif_skip
.Lkpre_skip_d:
	ds_read_b128 v[188:191], v174
	ds_read_b128 v[192:195], v173
	ds_read_b128 v[202:205], v172
	s_branch .LBB0_455

.LBB0_669:
	s_waitcnt lgkmcnt(0)
	s_andn2_b32 s2, s2, s8
	s_addk_i32 s5, 0x4000
	s_add_i32 s7, s7, -1
	s_cmp_lg_u32 s2, 0
	s_cbranch_scc0 .LBB0_698

.LBB0_681:
	s_flbit_i32_b32 s0, s2
	s_xor_b32 s0, s0, 31
	s_lshl_b32 s8, 1, s0
	s_waitcnt lgkmcnt(0)
	v_and_b32_e32 v2, s8, v136
	v_cmp_ne_u32_e64 s[38:39], 0, v2
	s_mov_b64 vcc, s[38:39]
	s_cbranch_vccz .LBB0_669
	s_and_b32 s1, s5, 0xc000
	s_lshl_b32 s9, s0, 6
	s_lshr_b32 s0, s0, 2
	s_xor_b32 s1, s1, 0x8000
	v_cvt_f32_u32_e32 v159, s0
	s_add_i32 s1, s1, 0
	v_add_u32_e32 v2, s1, v137
	v_add_u32_e32 v4, s1, v138
	v_add_u32_e32 v5, s1, v139
	v_add_u32_e32 v6, s1, v140
	s_or_b32 s10, s9, 32
	s_cmp_gt_i32 s10, s6
	v_add_u32_e32 v163, v2, v134
	v_add_u32_e32 v162, v4, v134
	v_add_u32_e32 v161, v5, v134
	v_add_u32_e32 v160, v6, v134
	v_add_u32_e32 v17, s1, v156
	v_add_u32_e32 v16, s1, v157
	s_cbranch_scc1 .Lkpre_skip_n
	ds_read_b128 v[4:7], v163 offset:4096
	ds_read_b128 v[188:191], v162 offset:4096
	ds_read_b128 v[192:195], v161 offset:4096
	ds_read_b128 v[202:205], v160 offset:4096
	s_and_b32 s0, s10, 0xe0
	v_or_b32_e32 v2, s0, v129
	v_cvt_f32_ubyte0_e32 v2, v2
	v_and_b32_e32 v2, 0x7fff0000, v2
	v_or_b32_sdwa v2, v2, v159 dst_sel:DWORD dst_unused:UNUSED_PAD src0_sel:DWORD src1_sel:WORD_1
	v_cndmask_b32_e64 v210, 0, v2, s[22:23]
	s_or_b32 s0, s9, 63
	s_cmp_lt_u32 s16, s0
	s_waitcnt lgkmcnt(3)
	s_setprio 1
	v_mfma_f32_32x32x16_bf16 v[82:97], v[4:7], v[106:109], 0
	s_cselect_b64 s[0:1], -1, 0
	s_sub_i32 s11, s16, s10
	s_cmp_gt_i32 s11, 0x3fffffe0
	v_add3_u32 v164, v16, v135, s69
	s_cselect_b64 s[12:13], -1, 0
	s_or_b64 s[0:1], s[0:1], s[12:13]
	s_and_b64 vcc, exec, s[0:1]
	s_waitcnt lgkmcnt(2)
	v_mfma_f32_32x32x16_bf16 v[82:97], v[188:191], v[98:101], v[82:97]
	s_waitcnt lgkmcnt(1)
	v_mfma_f32_32x32x16_bf16 v[82:97], v[192:195], v[102:105], v[82:97]
	s_waitcnt lgkmcnt(0)
	v_mfma_f32_32x32x16_bf16 v[82:97], v[202:205], v[110:113], v[82:97]
	v_mfma_f32_32x32x16_bf16 v[82:97], v[210:213], v[114:117], v[82:97]
	v_add3_u32 v2, v17, v135, s69
	ds_read_b64_tr_b16 v[118:119], v2
	ds_read_b64_tr_b16 v[120:121], v2 offset:1024
	ds_read_b64_tr_b16 v[12:13], v164
	ds_read_b64_tr_b16 v[14:15], v164 offset:1024
	ds_read_b64_tr_b16 v[8:9], v2 offset:2048
	ds_read_b64_tr_b16 v[10:11], v2 offset:3072
	ds_read_b64_tr_b16 v[4:5], v164 offset:2048
	ds_read_b64_tr_b16 v[6:7], v164 offset:3072
	ds_read_b128 v[188:191], v163
	ds_read_b128 v[192:195], v162
	ds_read_b128 v[202:205], v161
	s_cbranch_vccnz .LBB0_685
	v_cndmask_b32_e64 v2, 0, 1, s[38:39]
	v_cmp_ne_u32_e32 vcc, 0, v2
	s_cmp_lg_u64 vcc, exec
	s_cselect_b64 s[0:1], -1, 0
	s_cbranch_scc0 .LBB0_687
	v_cndmask_b32_e64 v82, v197, v82, s[38:39]
	v_cndmask_b32_e64 v83, v197, v83, s[38:39]
	v_cndmask_b32_e64 v84, v197, v84, s[38:39]
	v_cndmask_b32_e64 v85, v197, v85, s[38:39]
	v_cndmask_b32_e64 v86, v197, v86, s[38:39]
	v_cndmask_b32_e64 v87, v197, v87, s[38:39]
	v_cndmask_b32_e64 v88, v197, v88, s[38:39]
	v_cndmask_b32_e64 v89, v197, v89, s[38:39]
	v_cndmask_b32_e64 v90, v197, v90, s[38:39]
	v_cndmask_b32_e64 v91, v197, v91, s[38:39]
	v_cndmask_b32_e64 v92, v197, v92, s[38:39]
	v_cndmask_b32_e64 v93, v197, v93, s[38:39]
	v_cndmask_b32_e64 v94, v197, v94, s[38:39]
	v_cndmask_b32_e64 v95, v197, v95, s[38:39]
	v_cndmask_b32_e64 v96, v197, v96, s[38:39]
	v_cndmask_b32_e64 v97, v197, v97, s[38:39]
	s_branch .LBB0_687

.LBB0_690:
	s_cmp_gt_i32 s9, s6
	s_cbranch_scc1 .LBB0_669
	ds_read_b128 v[4:7], v160
	s_and_b32 s0, s9, 0xc0
	v_or_b32_e32 v2, s0, v129
	v_cvt_f32_ubyte0_e32 v2, v2
	v_and_b32_e32 v2, 0x7fff0000, v2
	v_or_b32_sdwa v2, v2, v159 dst_sel:DWORD dst_unused:UNUSED_PAD src0_sel:DWORD src1_sel:WORD_1
	v_cndmask_b32_e64 v210, 0, v2, s[22:23]
	s_or_b32 s0, s9, 31
	s_cmp_lt_i32 s16, s0
	s_waitcnt lgkmcnt(1)
	s_setprio 1
	v_mfma_f32_32x32x16_bf16 v[82:97], v[188:191], v[106:109], 0
	s_cselect_b64 s[0:1], -1, 0
	s_sub_i32 s10, s16, s9
	s_cmp_gt_i32 s10, 0x3fffffe0
	v_add3_u32 v16, v16, v135, s67
	s_cselect_b64 s[10:11], -1, 0
	s_or_b64 s[0:1], s[0:1], s[10:11]
	s_and_b64 vcc, exec, s[0:1]
	v_mfma_f32_32x32x16_bf16 v[82:97], v[192:195], v[98:101], v[82:97]
	v_mfma_f32_32x32x16_bf16 v[82:97], v[202:205], v[102:105], v[82:97]
	s_waitcnt lgkmcnt(0)
	v_mfma_f32_32x32x16_bf16 v[82:97], v[4:7], v[110:113], v[82:97]
	v_mfma_f32_32x32x16_bf16 v[82:97], v[210:213], v[114:117], v[82:97]
	v_add3_u32 v2, v17, v135, s67
	ds_read_b64_tr_b16 v[118:119], v2
	ds_read_b64_tr_b16 v[120:121], v2 offset:1024
	ds_read_b64_tr_b16 v[12:13], v16
	ds_read_b64_tr_b16 v[14:15], v16 offset:1024
	ds_read_b64_tr_b16 v[8:9], v2 offset:2048
	ds_read_b64_tr_b16 v[10:11], v2 offset:3072
	ds_read_b64_tr_b16 v[4:5], v16 offset:2048
	ds_read_b64_tr_b16 v[6:7], v16 offset:3072
	s_cbranch_vccnz .LBB0_693
	v_cndmask_b32_e64 v2, 0, 1, s[38:39]
	v_cmp_ne_u32_e32 vcc, 0, v2
	s_cmp_lg_u64 vcc, exec
	s_cselect_b64 s[0:1], -1, 0
	s_cbranch_scc0 .LBB0_695
	v_cndmask_b32_e64 v82, v197, v82, s[38:39]
	v_cndmask_b32_e64 v83, v197, v83, s[38:39]
	v_cndmask_b32_e64 v84, v197, v84, s[38:39]
	v_cndmask_b32_e64 v85, v197, v85, s[38:39]
	v_cndmask_b32_e64 v86, v197, v86, s[38:39]
	v_cndmask_b32_e64 v87, v197, v87, s[38:39]
	v_cndmask_b32_e64 v88, v197, v88, s[38:39]
	v_cndmask_b32_e64 v89, v197, v89, s[38:39]
	v_cndmask_b32_e64 v90, v197, v90, s[38:39]
	v_cndmask_b32_e64 v91, v197, v91, s[38:39]
	v_cndmask_b32_e64 v92, v197, v92, s[38:39]
	v_cndmask_b32_e64 v93, v197, v93, s[38:39]
	v_cndmask_b32_e64 v94, v197, v94, s[38:39]
	v_cndmask_b32_e64 v95, v197, v95, s[38:39]
	v_cndmask_b32_e64 v96, v197, v96, s[38:39]
	v_cndmask_b32_e64 v97, v197, v97, s[38:39]
	s_branch .LBB0_695
.Lkpre_skip_n:
	ds_read_b128 v[188:191], v163
	ds_read_b128 v[192:195], v162
	ds_read_b128 v[202:205], v161
	s_branch .LBB0_690
